# G1 u8 gate epilogue: two pre-exp multiplies folded into one constant, x256 folded into the reciprocal argument via fma (bit-identical), 2 of 8.5 VALU per element removed; plus static prio
# baseline (speedup 1.0000x reference)
.LBB0_298:
	s_and_b64 vcc, exec, s[4:5]
	s_cbranch_vccz .LBB0_300
	s_mov_b32 s98, 0x3b800000
	s_waitcnt lgkmcnt(0)
	v_mul_f32_e32 v2, 0xbcb8aa3b, v136
	v_exp_f32_e32 v4, v2
	v_mul_f32_e32 v6, 0xbcb8aa3b, v137
	v_exp_f32_e32 v6, v6
	v_fma_f32 v4, v4, s98, s98
	v_rcp_f32_e32 v4, v4
	v_mul_f32_e32 v8, 0xbcb8aa3b, v138
	v_exp_f32_e32 v8, v8
	v_min_f32_e32 v4, 0x437f0000, v4
	v_cvt_u32_f32_e32 v7, v4
	v_fma_f32 v4, v6, s98, s98
	v_rcp_f32_e32 v4, v4
	v_mul_f32_e32 v1, 0xbcb8aa3b, v140
	v_mul_f32_e32 v5, 0xbcb8aa3b, v141
	v_min_f32_e32 v4, 0x437f0000, v4
	v_mul_f32_e32 v6, 0xbcb8aa3b, v142
	v_cvt_u32_f32_e32 v9, v4
	v_fma_f32 v4, v8, s98, s98
	v_mul_f32_e32 v8, 0xbcb8aa3b, v143
	v_exp_f32_e32 v1, v1
	v_exp_f32_e32 v5, v5
	v_exp_f32_e32 v6, v6
	v_exp_f32_e32 v8, v8
	v_rcp_f32_e32 v4, v4
	v_mul_f32_e32 v10, 0xbcb8aa3b, v139
	v_fma_f32 v1, v1, s98, s98
	v_fma_f32 v5, v5, s98, s98
	v_rcp_f32_e32 v1, v1
	v_rcp_f32_e32 v5, v5
	v_fma_f32 v6, v6, s98, s98
	v_exp_f32_e32 v10, v10
	v_fma_f32 v8, v8, s98, s98
	v_rcp_f32_e32 v6, v6
	v_rcp_f32_e32 v8, v8
	v_min_f32_e32 v4, 0x437f0000, v4
	v_cvt_u32_f32_sdwa v11, v4 dst_sel:WORD_1 dst_unused:UNUSED_PAD src0_sel:DWORD
	v_fma_f32 v4, v10, s98, s98
	v_min_f32_e32 v1, 0x437f0000, v1
	v_min_f32_e32 v5, 0x437f0000, v5
	v_rcp_f32_e32 v4, v4
	v_cvt_u32_f32_e32 v1, v1
	v_cvt_u32_f32_e32 v5, v5
	v_min_f32_e32 v6, 0x437f0000, v6
	v_min_f32_e32 v8, 0x437f0000, v8
	v_cvt_u32_f32_sdwa v6, v6 dst_sel:WORD_1 dst_unused:UNUSED_PAD src0_sel:DWORD
	v_cvt_u32_f32_sdwa v8, v8 dst_sel:BYTE_3 dst_unused:UNUSED_PAD src0_sel:DWORD
	v_min_f32_e32 v4, 0x437f0000, v4
	v_lshl_or_b32 v1, v5, 8, v1
	v_cvt_u32_f32_sdwa v10, v4 dst_sel:BYTE_3 dst_unused:UNUSED_PAD src0_sel:DWORD
	v_or3_b32 v4, v1, v6, v8
	v_mul_f32_e32 v6, 0xbcb8aa3b, v128
	s_mul_i32 s4, s68, 24
	s_add_i32 s4, s4, s24
	v_exp_f32_e32 v6, v6
	s_ashr_i32 s5, s4, 31
	s_lshl_b64 s[4:5], s[4:5], 16
	v_lshl_or_b32 v1, v9, 8, v7
	v_lshl_add_u64 v[2:3], v[156:157], 0, s[4:5]
	v_or3_b32 v5, v1, v11, v10
	global_store_dwordx2 v[2:3], v[4:5], off
	v_fma_f32 v4, v6, s98, s98
	v_rcp_f32_e32 v4, v4
	v_mul_f32_e32 v6, 0xbcb8aa3b, v129
	v_exp_f32_e32 v6, v6
	v_min_f32_e32 v4, 0x437f0000, v4
	v_cvt_u32_f32_e32 v7, v4
	v_fma_f32 v4, v6, s98, s98
	v_rcp_f32_e32 v4, v4
	v_mul_f32_e32 v8, 0xbcb8aa3b, v130
	v_exp_f32_e32 v8, v8
	v_mul_f32_e32 v1, 0xbcb8aa3b, v132
	v_mul_f32_e32 v5, 0xbcb8aa3b, v133
	v_min_f32_e32 v4, 0x437f0000, v4
	v_mul_f32_e32 v6, 0xbcb8aa3b, v134
	v_cvt_u32_f32_e32 v9, v4
	v_fma_f32 v4, v8, s98, s98
	v_mul_f32_e32 v8, 0xbcb8aa3b, v135
	v_exp_f32_e32 v1, v1
	v_exp_f32_e32 v5, v5
	v_exp_f32_e32 v6, v6
	v_exp_f32_e32 v8, v8
	v_rcp_f32_e32 v4, v4
	v_mul_f32_e32 v10, 0xbcb8aa3b, v131
	v_fma_f32 v1, v1, s98, s98
	v_fma_f32 v5, v5, s98, s98
	v_rcp_f32_e32 v1, v1
	v_rcp_f32_e32 v5, v5
	v_fma_f32 v6, v6, s98, s98
	v_exp_f32_e32 v10, v10
	v_fma_f32 v8, v8, s98, s98
	v_rcp_f32_e32 v6, v6
	v_rcp_f32_e32 v8, v8
	v_min_f32_e32 v4, 0x437f0000, v4
	v_cvt_u32_f32_sdwa v11, v4 dst_sel:WORD_1 dst_unused:UNUSED_PAD src0_sel:DWORD
	v_fma_f32 v4, v10, s98, s98
	v_min_f32_e32 v1, 0x437f0000, v1
	v_min_f32_e32 v5, 0x437f0000, v5
	v_rcp_f32_e32 v4, v4
	v_cvt_u32_f32_e32 v1, v1
	v_cvt_u32_f32_e32 v5, v5
	v_min_f32_e32 v6, 0x437f0000, v6
	v_min_f32_e32 v8, 0x437f0000, v8
	v_cvt_u32_f32_sdwa v6, v6 dst_sel:WORD_1 dst_unused:UNUSED_PAD src0_sel:DWORD
	v_cvt_u32_f32_sdwa v8, v8 dst_sel:BYTE_3 dst_unused:UNUSED_PAD src0_sel:DWORD
	v_min_f32_e32 v4, 0x437f0000, v4
	v_lshl_or_b32 v1, v5, 8, v1
	v_cvt_u32_f32_sdwa v10, v4 dst_sel:BYTE_3 dst_unused:UNUSED_PAD src0_sel:DWORD
	v_or3_b32 v4, v1, v6, v8
	v_mul_f32_e32 v6, 0xbcb8aa3b, v120
	v_exp_f32_e32 v6, v6
	v_lshl_or_b32 v1, v9, 8, v7
	v_or3_b32 v5, v1, v11, v10
	global_store_dwordx2 v[2:3], v[4:5], off offset:512
	v_fma_f32 v4, v6, s98, s98
	v_rcp_f32_e32 v4, v4
	v_mul_f32_e32 v6, 0xbcb8aa3b, v121
	v_exp_f32_e32 v6, v6
	v_min_f32_e32 v4, 0x437f0000, v4
	v_cvt_u32_f32_e32 v7, v4
	v_fma_f32 v4, v6, s98, s98
	v_rcp_f32_e32 v4, v4
	v_mul_f32_e32 v8, 0xbcb8aa3b, v122
	v_exp_f32_e32 v8, v8
	v_mul_f32_e32 v1, 0xbcb8aa3b, v124
	v_mul_f32_e32 v5, 0xbcb8aa3b, v125
	v_min_f32_e32 v4, 0x437f0000, v4
	v_mul_f32_e32 v6, 0xbcb8aa3b, v126
	v_cvt_u32_f32_e32 v9, v4
	v_fma_f32 v4, v8, s98, s98
	v_mul_f32_e32 v8, 0xbcb8aa3b, v127
	v_exp_f32_e32 v1, v1
	v_exp_f32_e32 v5, v5
	v_exp_f32_e32 v6, v6
	v_exp_f32_e32 v8, v8
	v_rcp_f32_e32 v4, v4
	v_mul_f32_e32 v10, 0xbcb8aa3b, v123
	v_fma_f32 v1, v1, s98, s98
	v_fma_f32 v5, v5, s98, s98
	v_rcp_f32_e32 v1, v1
	v_rcp_f32_e32 v5, v5
	v_fma_f32 v6, v6, s98, s98
	v_exp_f32_e32 v10, v10
	v_fma_f32 v8, v8, s98, s98
	v_rcp_f32_e32 v6, v6
	v_rcp_f32_e32 v8, v8
	v_min_f32_e32 v4, 0x437f0000, v4
	v_cvt_u32_f32_sdwa v11, v4 dst_sel:WORD_1 dst_unused:UNUSED_PAD src0_sel:DWORD
	v_fma_f32 v4, v10, s98, s98
	v_min_f32_e32 v1, 0x437f0000, v1
	v_min_f32_e32 v5, 0x437f0000, v5
	v_rcp_f32_e32 v4, v4
	v_cvt_u32_f32_e32 v1, v1
	v_cvt_u32_f32_e32 v5, v5
	v_min_f32_e32 v6, 0x437f0000, v6
	v_min_f32_e32 v8, 0x437f0000, v8
	v_cvt_u32_f32_sdwa v6, v6 dst_sel:WORD_1 dst_unused:UNUSED_PAD src0_sel:DWORD
	v_cvt_u32_f32_sdwa v8, v8 dst_sel:BYTE_3 dst_unused:UNUSED_PAD src0_sel:DWORD
	v_min_f32_e32 v4, 0x437f0000, v4
	v_lshl_or_b32 v1, v5, 8, v1
	v_cvt_u32_f32_sdwa v10, v4 dst_sel:BYTE_3 dst_unused:UNUSED_PAD src0_sel:DWORD
	v_or3_b32 v4, v1, v6, v8
	v_mul_f32_e32 v6, 0xbcb8aa3b, v112
	v_exp_f32_e32 v6, v6
	v_lshl_or_b32 v1, v9, 8, v7
	v_or3_b32 v5, v1, v11, v10
	global_store_dwordx2 v[2:3], v[4:5], off offset:1024
	v_fma_f32 v4, v6, s98, s98
	v_rcp_f32_e32 v4, v4
	v_mul_f32_e32 v6, 0xbcb8aa3b, v113
	v_exp_f32_e32 v6, v6
	v_min_f32_e32 v4, 0x437f0000, v4
	v_cvt_u32_f32_e32 v7, v4
	v_fma_f32 v4, v6, s98, s98
	v_rcp_f32_e32 v4, v4
	v_mul_f32_e32 v8, 0xbcb8aa3b, v114
	v_exp_f32_e32 v8, v8
	v_mul_f32_e32 v1, 0xbcb8aa3b, v116
	v_mul_f32_e32 v5, 0xbcb8aa3b, v117
	v_min_f32_e32 v4, 0x437f0000, v4
	v_mul_f32_e32 v6, 0xbcb8aa3b, v118
	v_cvt_u32_f32_e32 v9, v4
	v_fma_f32 v4, v8, s98, s98
	v_mul_f32_e32 v8, 0xbcb8aa3b, v119
	v_exp_f32_e32 v1, v1
	v_exp_f32_e32 v5, v5
	v_exp_f32_e32 v6, v6
	v_exp_f32_e32 v8, v8
	v_rcp_f32_e32 v4, v4
	v_mul_f32_e32 v10, 0xbcb8aa3b, v115
	v_fma_f32 v1, v1, s98, s98
	v_fma_f32 v5, v5, s98, s98
	v_rcp_f32_e32 v1, v1
	v_rcp_f32_e32 v5, v5
	v_fma_f32 v6, v6, s98, s98
	v_exp_f32_e32 v10, v10
	v_fma_f32 v8, v8, s98, s98
	v_rcp_f32_e32 v6, v6
	v_rcp_f32_e32 v8, v8
	v_min_f32_e32 v4, 0x437f0000, v4
	v_cvt_u32_f32_sdwa v11, v4 dst_sel:WORD_1 dst_unused:UNUSED_PAD src0_sel:DWORD
	v_fma_f32 v4, v10, s98, s98
	v_min_f32_e32 v1, 0x437f0000, v1
	v_min_f32_e32 v5, 0x437f0000, v5
	v_rcp_f32_e32 v4, v4
	v_cvt_u32_f32_e32 v1, v1
	v_cvt_u32_f32_e32 v5, v5
	v_min_f32_e32 v6, 0x437f0000, v6
	v_min_f32_e32 v8, 0x437f0000, v8
	v_cvt_u32_f32_sdwa v6, v6 dst_sel:WORD_1 dst_unused:UNUSED_PAD src0_sel:DWORD
	v_cvt_u32_f32_sdwa v8, v8 dst_sel:BYTE_3 dst_unused:UNUSED_PAD src0_sel:DWORD
	v_min_f32_e32 v4, 0x437f0000, v4
	v_lshl_or_b32 v1, v5, 8, v1
	v_cvt_u32_f32_sdwa v10, v4 dst_sel:BYTE_3 dst_unused:UNUSED_PAD src0_sel:DWORD
	v_or3_b32 v4, v1, v6, v8
	v_mul_f32_e32 v6, 0xbcb8aa3b, v104
	v_exp_f32_e32 v6, v6
	v_lshl_or_b32 v1, v9, 8, v7
	v_or3_b32 v5, v1, v11, v10
	global_store_dwordx2 v[2:3], v[4:5], off offset:1536
	v_fma_f32 v4, v6, s98, s98
	v_rcp_f32_e32 v4, v4
	v_mul_f32_e32 v6, 0xbcb8aa3b, v105
	v_exp_f32_e32 v6, v6
	v_min_f32_e32 v4, 0x437f0000, v4
	v_cvt_u32_f32_e32 v7, v4
	v_fma_f32 v4, v6, s98, s98
	v_rcp_f32_e32 v4, v4
	v_mul_f32_e32 v8, 0xbcb8aa3b, v106
	v_exp_f32_e32 v8, v8
	v_mul_f32_e32 v1, 0xbcb8aa3b, v108
	v_mul_f32_e32 v5, 0xbcb8aa3b, v109
	v_min_f32_e32 v4, 0x437f0000, v4
	v_mul_f32_e32 v6, 0xbcb8aa3b, v110
	v_cvt_u32_f32_e32 v9, v4
	v_fma_f32 v4, v8, s98, s98
	v_mul_f32_e32 v8, 0xbcb8aa3b, v111
	v_exp_f32_e32 v1, v1
	v_exp_f32_e32 v5, v5
	v_exp_f32_e32 v6, v6
	v_exp_f32_e32 v8, v8
	v_rcp_f32_e32 v4, v4
	v_mul_f32_e32 v10, 0xbcb8aa3b, v107
	v_fma_f32 v1, v1, s98, s98
	v_fma_f32 v5, v5, s98, s98
	v_rcp_f32_e32 v1, v1
	v_rcp_f32_e32 v5, v5
	v_fma_f32 v6, v6, s98, s98
	v_exp_f32_e32 v10, v10
	v_fma_f32 v8, v8, s98, s98
	v_rcp_f32_e32 v6, v6
	v_rcp_f32_e32 v8, v8
	v_min_f32_e32 v4, 0x437f0000, v4
	v_cvt_u32_f32_sdwa v11, v4 dst_sel:WORD_1 dst_unused:UNUSED_PAD src0_sel:DWORD
	v_fma_f32 v4, v10, s98, s98
	v_min_f32_e32 v1, 0x437f0000, v1
	v_min_f32_e32 v5, 0x437f0000, v5
	v_rcp_f32_e32 v4, v4
	v_cvt_u32_f32_e32 v1, v1
	v_cvt_u32_f32_e32 v5, v5
	v_min_f32_e32 v6, 0x437f0000, v6
	v_min_f32_e32 v8, 0x437f0000, v8
	v_cvt_u32_f32_sdwa v6, v6 dst_sel:WORD_1 dst_unused:UNUSED_PAD src0_sel:DWORD
	v_cvt_u32_f32_sdwa v8, v8 dst_sel:BYTE_3 dst_unused:UNUSED_PAD src0_sel:DWORD
	v_min_f32_e32 v4, 0x437f0000, v4
	v_lshl_or_b32 v1, v5, 8, v1
	v_cvt_u32_f32_sdwa v10, v4 dst_sel:BYTE_3 dst_unused:UNUSED_PAD src0_sel:DWORD
	v_or3_b32 v4, v1, v6, v8
	v_mul_f32_e32 v6, 0xbcb8aa3b, v96
	v_exp_f32_e32 v6, v6
	v_lshl_or_b32 v1, v9, 8, v7
	v_or3_b32 v5, v1, v11, v10
	global_store_dwordx2 v[2:3], v[4:5], off offset:2048
	v_fma_f32 v4, v6, s98, s98
	v_rcp_f32_e32 v4, v4
	v_mul_f32_e32 v6, 0xbcb8aa3b, v97
	v_exp_f32_e32 v6, v6
	v_min_f32_e32 v4, 0x437f0000, v4
	v_cvt_u32_f32_e32 v7, v4
	v_fma_f32 v4, v6, s98, s98
	v_rcp_f32_e32 v4, v4
	v_mul_f32_e32 v8, 0xbcb8aa3b, v98
	v_exp_f32_e32 v8, v8
	v_mul_f32_e32 v1, 0xbcb8aa3b, v100
	v_mul_f32_e32 v5, 0xbcb8aa3b, v101
	v_min_f32_e32 v4, 0x437f0000, v4
	v_mul_f32_e32 v6, 0xbcb8aa3b, v102
	v_cvt_u32_f32_e32 v9, v4
	v_fma_f32 v4, v8, s98, s98
	v_mul_f32_e32 v8, 0xbcb8aa3b, v103
	v_exp_f32_e32 v1, v1
	v_exp_f32_e32 v5, v5
	v_exp_f32_e32 v6, v6
	v_exp_f32_e32 v8, v8
	v_rcp_f32_e32 v4, v4
	v_mul_f32_e32 v10, 0xbcb8aa3b, v99
	v_fma_f32 v1, v1, s98, s98
	v_fma_f32 v5, v5, s98, s98
	v_rcp_f32_e32 v1, v1
	v_rcp_f32_e32 v5, v5
	v_fma_f32 v6, v6, s98, s98
	v_exp_f32_e32 v10, v10
	v_fma_f32 v8, v8, s98, s98
	v_rcp_f32_e32 v6, v6
	v_rcp_f32_e32 v8, v8
	v_min_f32_e32 v4, 0x437f0000, v4
	v_cvt_u32_f32_sdwa v11, v4 dst_sel:WORD_1 dst_unused:UNUSED_PAD src0_sel:DWORD
	v_fma_f32 v4, v10, s98, s98
	v_min_f32_e32 v1, 0x437f0000, v1
	v_min_f32_e32 v5, 0x437f0000, v5
	v_rcp_f32_e32 v4, v4
	v_cvt_u32_f32_e32 v1, v1
	v_cvt_u32_f32_e32 v5, v5
	v_min_f32_e32 v6, 0x437f0000, v6
	v_min_f32_e32 v8, 0x437f0000, v8
	v_cvt_u32_f32_sdwa v6, v6 dst_sel:WORD_1 dst_unused:UNUSED_PAD src0_sel:DWORD
	v_cvt_u32_f32_sdwa v8, v8 dst_sel:BYTE_3 dst_unused:UNUSED_PAD src0_sel:DWORD
	v_min_f32_e32 v4, 0x437f0000, v4
	v_lshl_or_b32 v1, v5, 8, v1
	v_cvt_u32_f32_sdwa v10, v4 dst_sel:BYTE_3 dst_unused:UNUSED_PAD src0_sel:DWORD
	v_or3_b32 v4, v1, v6, v8
	v_mul_f32_e32 v6, 0xbcb8aa3b, v88
	v_exp_f32_e32 v6, v6
	v_lshl_or_b32 v1, v9, 8, v7
	v_or3_b32 v5, v1, v11, v10
	global_store_dwordx2 v[2:3], v[4:5], off offset:2560
	v_fma_f32 v4, v6, s98, s98
	v_rcp_f32_e32 v4, v4
	v_mul_f32_e32 v6, 0xbcb8aa3b, v89
	v_exp_f32_e32 v6, v6
	v_min_f32_e32 v4, 0x437f0000, v4
	v_cvt_u32_f32_e32 v7, v4
	v_fma_f32 v4, v6, s98, s98
	v_rcp_f32_e32 v4, v4
	v_mul_f32_e32 v8, 0xbcb8aa3b, v90
	v_exp_f32_e32 v8, v8
	v_mul_f32_e32 v1, 0xbcb8aa3b, v92
	v_mul_f32_e32 v5, 0xbcb8aa3b, v93
	v_min_f32_e32 v4, 0x437f0000, v4
	v_mul_f32_e32 v6, 0xbcb8aa3b, v94
	v_cvt_u32_f32_e32 v9, v4
	v_fma_f32 v4, v8, s98, s98
	v_mul_f32_e32 v8, 0xbcb8aa3b, v95
	v_exp_f32_e32 v1, v1
	v_exp_f32_e32 v5, v5
	v_exp_f32_e32 v6, v6
	v_exp_f32_e32 v8, v8
	v_rcp_f32_e32 v4, v4
	v_mul_f32_e32 v10, 0xbcb8aa3b, v91
	v_fma_f32 v1, v1, s98, s98
	v_fma_f32 v5, v5, s98, s98
	v_rcp_f32_e32 v1, v1
	v_rcp_f32_e32 v5, v5
	v_fma_f32 v6, v6, s98, s98
	v_exp_f32_e32 v10, v10
	v_fma_f32 v8, v8, s98, s98
	v_rcp_f32_e32 v6, v6
	v_rcp_f32_e32 v8, v8
	v_min_f32_e32 v4, 0x437f0000, v4
	v_cvt_u32_f32_sdwa v11, v4 dst_sel:WORD_1 dst_unused:UNUSED_PAD src0_sel:DWORD
	v_fma_f32 v4, v10, s98, s98
	v_min_f32_e32 v1, 0x437f0000, v1
	v_min_f32_e32 v5, 0x437f0000, v5
	v_rcp_f32_e32 v4, v4
	v_cvt_u32_f32_e32 v1, v1
	v_cvt_u32_f32_e32 v5, v5
	v_min_f32_e32 v6, 0x437f0000, v6
	v_min_f32_e32 v8, 0x437f0000, v8
	v_cvt_u32_f32_sdwa v6, v6 dst_sel:WORD_1 dst_unused:UNUSED_PAD src0_sel:DWORD
	v_cvt_u32_f32_sdwa v8, v8 dst_sel:BYTE_3 dst_unused:UNUSED_PAD src0_sel:DWORD
	v_min_f32_e32 v4, 0x437f0000, v4
	v_lshl_or_b32 v1, v5, 8, v1
	v_cvt_u32_f32_sdwa v10, v4 dst_sel:BYTE_3 dst_unused:UNUSED_PAD src0_sel:DWORD
	v_or3_b32 v4, v1, v6, v8
	v_mul_f32_e32 v6, 0xbcb8aa3b, v80
	v_exp_f32_e32 v6, v6
	v_lshl_or_b32 v1, v9, 8, v7
	v_or3_b32 v5, v1, v11, v10
	global_store_dwordx2 v[2:3], v[4:5], off offset:3072
	v_fma_f32 v4, v6, s98, s98
	v_rcp_f32_e32 v4, v4
	v_mul_f32_e32 v6, 0xbcb8aa3b, v81
	v_exp_f32_e32 v6, v6
	v_min_f32_e32 v4, 0x437f0000, v4
	v_cvt_u32_f32_e32 v7, v4
	v_fma_f32 v4, v6, s98, s98
	v_rcp_f32_e32 v4, v4
	v_mul_f32_e32 v8, 0xbcb8aa3b, v82
	v_exp_f32_e32 v8, v8
	v_mul_f32_e32 v1, 0xbcb8aa3b, v84
	v_mul_f32_e32 v5, 0xbcb8aa3b, v85
	v_min_f32_e32 v4, 0x437f0000, v4
	v_mul_f32_e32 v6, 0xbcb8aa3b, v86
	v_cvt_u32_f32_e32 v9, v4
	v_fma_f32 v4, v8, s98, s98
	v_mul_f32_e32 v8, 0xbcb8aa3b, v87
	v_exp_f32_e32 v1, v1
	v_exp_f32_e32 v5, v5
	v_exp_f32_e32 v6, v6
	v_exp_f32_e32 v8, v8
	v_rcp_f32_e32 v4, v4
	v_mul_f32_e32 v10, 0xbcb8aa3b, v83
	v_fma_f32 v1, v1, s98, s98
	v_fma_f32 v5, v5, s98, s98
	v_rcp_f32_e32 v1, v1
	v_rcp_f32_e32 v5, v5
	v_fma_f32 v6, v6, s98, s98
	v_exp_f32_e32 v10, v10
	v_fma_f32 v8, v8, s98, s98
	v_rcp_f32_e32 v6, v6
	v_rcp_f32_e32 v8, v8
	v_min_f32_e32 v4, 0x437f0000, v4
	v_cvt_u32_f32_sdwa v11, v4 dst_sel:WORD_1 dst_unused:UNUSED_PAD src0_sel:DWORD
	v_fma_f32 v4, v10, s98, s98
	v_min_f32_e32 v1, 0x437f0000, v1
	v_min_f32_e32 v5, 0x437f0000, v5
	v_rcp_f32_e32 v4, v4
	v_cvt_u32_f32_e32 v1, v1
	v_cvt_u32_f32_e32 v5, v5
	v_min_f32_e32 v6, 0x437f0000, v6
	v_min_f32_e32 v8, 0x437f0000, v8
	v_cvt_u32_f32_sdwa v6, v6 dst_sel:WORD_1 dst_unused:UNUSED_PAD src0_sel:DWORD
	v_cvt_u32_f32_sdwa v8, v8 dst_sel:BYTE_3 dst_unused:UNUSED_PAD src0_sel:DWORD
	v_min_f32_e32 v4, 0x437f0000, v4
	v_lshl_or_b32 v1, v5, 8, v1
	v_cvt_u32_f32_sdwa v10, v4 dst_sel:BYTE_3 dst_unused:UNUSED_PAD src0_sel:DWORD
	v_or3_b32 v4, v1, v6, v8
	v_mul_f32_e32 v6, 0xbcb8aa3b, v72
	v_exp_f32_e32 v6, v6
	v_lshl_or_b32 v1, v9, 8, v7
	v_or3_b32 v5, v1, v11, v10
	global_store_dwordx2 v[2:3], v[4:5], off offset:3584
	v_fma_f32 v4, v6, s98, s98
	v_rcp_f32_e32 v4, v4
	v_mul_f32_e32 v6, 0xbcb8aa3b, v73
	v_exp_f32_e32 v6, v6
	v_min_f32_e32 v4, 0x437f0000, v4
	v_cvt_u32_f32_e32 v7, v4
	v_fma_f32 v4, v6, s98, s98
	v_rcp_f32_e32 v4, v4
	v_mul_f32_e32 v8, 0xbcb8aa3b, v74
	v_exp_f32_e32 v8, v8
	v_mul_f32_e32 v1, 0xbcb8aa3b, v76
	v_mul_f32_e32 v5, 0xbcb8aa3b, v77
	v_min_f32_e32 v4, 0x437f0000, v4
	v_mul_f32_e32 v6, 0xbcb8aa3b, v78
	v_cvt_u32_f32_e32 v9, v4
	v_fma_f32 v4, v8, s98, s98
	v_mul_f32_e32 v8, 0xbcb8aa3b, v79
	v_exp_f32_e32 v1, v1
	v_exp_f32_e32 v5, v5
	v_exp_f32_e32 v6, v6
	v_exp_f32_e32 v8, v8
	v_rcp_f32_e32 v4, v4
	v_mul_f32_e32 v10, 0xbcb8aa3b, v75
	v_fma_f32 v1, v1, s98, s98
	v_fma_f32 v5, v5, s98, s98
	v_rcp_f32_e32 v1, v1
	v_rcp_f32_e32 v5, v5
	v_fma_f32 v6, v6, s98, s98
	v_exp_f32_e32 v10, v10
	v_fma_f32 v8, v8, s98, s98
	v_rcp_f32_e32 v6, v6
	v_rcp_f32_e32 v8, v8
	v_min_f32_e32 v4, 0x437f0000, v4
	v_cvt_u32_f32_sdwa v11, v4 dst_sel:WORD_1 dst_unused:UNUSED_PAD src0_sel:DWORD
	v_fma_f32 v4, v10, s98, s98
	v_min_f32_e32 v1, 0x437f0000, v1
	v_min_f32_e32 v5, 0x437f0000, v5
	v_rcp_f32_e32 v4, v4
	v_cvt_u32_f32_e32 v1, v1
	v_cvt_u32_f32_e32 v5, v5
	v_min_f32_e32 v6, 0x437f0000, v6
	v_min_f32_e32 v8, 0x437f0000, v8
	v_cvt_u32_f32_sdwa v6, v6 dst_sel:WORD_1 dst_unused:UNUSED_PAD src0_sel:DWORD
	v_cvt_u32_f32_sdwa v8, v8 dst_sel:BYTE_3 dst_unused:UNUSED_PAD src0_sel:DWORD
	v_min_f32_e32 v4, 0x437f0000, v4
	v_lshl_or_b32 v1, v5, 8, v1
	v_cvt_u32_f32_sdwa v10, v4 dst_sel:BYTE_3 dst_unused:UNUSED_PAD src0_sel:DWORD
	v_or3_b32 v4, v1, v6, v8
	v_mul_f32_e32 v6, 0xbcb8aa3b, v64
	v_exp_f32_e32 v6, v6
	v_lshl_or_b32 v1, v9, 8, v7
	v_add_co_u32_e32 v2, vcc, s56, v2
	v_or3_b32 v5, v1, v11, v10
	s_nop 0
	v_addc_co_u32_e32 v3, vcc, 0, v3, vcc
	global_store_dwordx2 v[2:3], v[4:5], off
	v_fma_f32 v4, v6, s98, s98
	v_rcp_f32_e32 v4, v4
	v_mul_f32_e32 v6, 0xbcb8aa3b, v65
	v_exp_f32_e32 v6, v6
	v_min_f32_e32 v4, 0x437f0000, v4
	v_cvt_u32_f32_e32 v7, v4
	v_fma_f32 v4, v6, s98, s98
	v_rcp_f32_e32 v4, v4
	v_mul_f32_e32 v8, 0xbcb8aa3b, v66
	v_exp_f32_e32 v8, v8
	v_mul_f32_e32 v1, 0xbcb8aa3b, v68
	v_mul_f32_e32 v5, 0xbcb8aa3b, v69
	v_min_f32_e32 v4, 0x437f0000, v4
	v_mul_f32_e32 v6, 0xbcb8aa3b, v70
	v_cvt_u32_f32_e32 v9, v4
	v_fma_f32 v4, v8, s98, s98
	v_mul_f32_e32 v8, 0xbcb8aa3b, v71
	v_exp_f32_e32 v1, v1
	v_exp_f32_e32 v5, v5
	v_exp_f32_e32 v6, v6
	v_exp_f32_e32 v8, v8
	v_rcp_f32_e32 v4, v4
	v_mul_f32_e32 v10, 0xbcb8aa3b, v67
	v_fma_f32 v1, v1, s98, s98
	v_fma_f32 v5, v5, s98, s98
	v_rcp_f32_e32 v1, v1
	v_rcp_f32_e32 v5, v5
	v_fma_f32 v6, v6, s98, s98
	v_exp_f32_e32 v10, v10
	v_fma_f32 v8, v8, s98, s98
	v_rcp_f32_e32 v6, v6
	v_rcp_f32_e32 v8, v8
	v_min_f32_e32 v4, 0x437f0000, v4
	v_cvt_u32_f32_sdwa v11, v4 dst_sel:WORD_1 dst_unused:UNUSED_PAD src0_sel:DWORD
	v_fma_f32 v4, v10, s98, s98
	v_min_f32_e32 v1, 0x437f0000, v1
	v_min_f32_e32 v5, 0x437f0000, v5
	v_rcp_f32_e32 v4, v4
	v_cvt_u32_f32_e32 v1, v1
	v_cvt_u32_f32_e32 v5, v5
	v_min_f32_e32 v6, 0x437f0000, v6
	v_min_f32_e32 v8, 0x437f0000, v8
	v_cvt_u32_f32_sdwa v6, v6 dst_sel:WORD_1 dst_unused:UNUSED_PAD src0_sel:DWORD
	v_cvt_u32_f32_sdwa v8, v8 dst_sel:BYTE_3 dst_unused:UNUSED_PAD src0_sel:DWORD
	v_min_f32_e32 v4, 0x437f0000, v4
	v_lshl_or_b32 v1, v5, 8, v1
	v_cvt_u32_f32_sdwa v10, v4 dst_sel:BYTE_3 dst_unused:UNUSED_PAD src0_sel:DWORD
	v_or3_b32 v4, v1, v6, v8
	v_mul_f32_e32 v6, 0xbcb8aa3b, v56
	v_exp_f32_e32 v6, v6
	v_lshl_or_b32 v1, v9, 8, v7
	v_or3_b32 v5, v1, v11, v10
	global_store_dwordx2 v[2:3], v[4:5], off offset:512
	v_fma_f32 v4, v6, s98, s98
	v_rcp_f32_e32 v4, v4
	v_mul_f32_e32 v6, 0xbcb8aa3b, v57
	v_exp_f32_e32 v6, v6
	v_min_f32_e32 v4, 0x437f0000, v4
	v_cvt_u32_f32_e32 v7, v4
	v_fma_f32 v4, v6, s98, s98
	v_rcp_f32_e32 v4, v4
	v_mul_f32_e32 v8, 0xbcb8aa3b, v58
	v_exp_f32_e32 v8, v8
	v_mul_f32_e32 v1, 0xbcb8aa3b, v60
	v_mul_f32_e32 v5, 0xbcb8aa3b, v61
	v_min_f32_e32 v4, 0x437f0000, v4
	v_mul_f32_e32 v6, 0xbcb8aa3b, v62
	v_cvt_u32_f32_e32 v9, v4
	v_fma_f32 v4, v8, s98, s98
	v_mul_f32_e32 v8, 0xbcb8aa3b, v63
	v_exp_f32_e32 v1, v1
	v_exp_f32_e32 v5, v5
	v_exp_f32_e32 v6, v6
	v_exp_f32_e32 v8, v8
	v_rcp_f32_e32 v4, v4
	v_mul_f32_e32 v10, 0xbcb8aa3b, v59
	v_fma_f32 v1, v1, s98, s98
	v_fma_f32 v5, v5, s98, s98
	v_rcp_f32_e32 v1, v1
	v_rcp_f32_e32 v5, v5
	v_fma_f32 v6, v6, s98, s98
	v_exp_f32_e32 v10, v10
	v_fma_f32 v8, v8, s98, s98
	v_rcp_f32_e32 v6, v6
	v_rcp_f32_e32 v8, v8
	v_min_f32_e32 v4, 0x437f0000, v4
	v_cvt_u32_f32_sdwa v11, v4 dst_sel:WORD_1 dst_unused:UNUSED_PAD src0_sel:DWORD
	v_fma_f32 v4, v10, s98, s98
	v_min_f32_e32 v1, 0x437f0000, v1
	v_min_f32_e32 v5, 0x437f0000, v5
	v_rcp_f32_e32 v4, v4
	v_cvt_u32_f32_e32 v1, v1
	v_cvt_u32_f32_e32 v5, v5
	v_min_f32_e32 v6, 0x437f0000, v6
	v_min_f32_e32 v8, 0x437f0000, v8
	v_cvt_u32_f32_sdwa v6, v6 dst_sel:WORD_1 dst_unused:UNUSED_PAD src0_sel:DWORD
	v_cvt_u32_f32_sdwa v8, v8 dst_sel:BYTE_3 dst_unused:UNUSED_PAD src0_sel:DWORD
	v_min_f32_e32 v4, 0x437f0000, v4
	v_lshl_or_b32 v1, v5, 8, v1
	v_cvt_u32_f32_sdwa v10, v4 dst_sel:BYTE_3 dst_unused:UNUSED_PAD src0_sel:DWORD
	v_or3_b32 v4, v1, v6, v8
	v_mul_f32_e32 v6, 0xbcb8aa3b, v48
	v_exp_f32_e32 v6, v6
	v_lshl_or_b32 v1, v9, 8, v7
	v_or3_b32 v5, v1, v11, v10
	global_store_dwordx2 v[2:3], v[4:5], off offset:1024
	v_fma_f32 v4, v6, s98, s98
	v_rcp_f32_e32 v4, v4
	v_mul_f32_e32 v6, 0xbcb8aa3b, v49
	v_exp_f32_e32 v6, v6
	v_min_f32_e32 v4, 0x437f0000, v4
	v_cvt_u32_f32_e32 v7, v4
	v_fma_f32 v4, v6, s98, s98
	v_rcp_f32_e32 v4, v4
	v_mul_f32_e32 v8, 0xbcb8aa3b, v50
	v_exp_f32_e32 v8, v8
	v_mul_f32_e32 v1, 0xbcb8aa3b, v52
	v_mul_f32_e32 v5, 0xbcb8aa3b, v53
	v_min_f32_e32 v4, 0x437f0000, v4
	v_mul_f32_e32 v6, 0xbcb8aa3b, v54
	v_cvt_u32_f32_e32 v9, v4
	v_fma_f32 v4, v8, s98, s98
	v_mul_f32_e32 v8, 0xbcb8aa3b, v55
	v_exp_f32_e32 v1, v1
	v_exp_f32_e32 v5, v5
	v_exp_f32_e32 v6, v6
	v_exp_f32_e32 v8, v8
	v_rcp_f32_e32 v4, v4
	v_mul_f32_e32 v10, 0xbcb8aa3b, v51
	v_fma_f32 v1, v1, s98, s98
	v_fma_f32 v5, v5, s98, s98
	v_rcp_f32_e32 v1, v1
	v_rcp_f32_e32 v5, v5
	v_fma_f32 v6, v6, s98, s98
	v_exp_f32_e32 v10, v10
	v_fma_f32 v8, v8, s98, s98
	v_rcp_f32_e32 v6, v6
	v_rcp_f32_e32 v8, v8
	v_min_f32_e32 v4, 0x437f0000, v4
	v_cvt_u32_f32_sdwa v11, v4 dst_sel:WORD_1 dst_unused:UNUSED_PAD src0_sel:DWORD
	v_fma_f32 v4, v10, s98, s98
	v_min_f32_e32 v1, 0x437f0000, v1
	v_min_f32_e32 v5, 0x437f0000, v5
	v_rcp_f32_e32 v4, v4
	v_cvt_u32_f32_e32 v1, v1
	v_cvt_u32_f32_e32 v5, v5
	v_min_f32_e32 v6, 0x437f0000, v6
	v_min_f32_e32 v8, 0x437f0000, v8
	v_cvt_u32_f32_sdwa v6, v6 dst_sel:WORD_1 dst_unused:UNUSED_PAD src0_sel:DWORD
	v_cvt_u32_f32_sdwa v8, v8 dst_sel:BYTE_3 dst_unused:UNUSED_PAD src0_sel:DWORD
	v_min_f32_e32 v4, 0x437f0000, v4
	v_lshl_or_b32 v1, v5, 8, v1
	v_cvt_u32_f32_sdwa v10, v4 dst_sel:BYTE_3 dst_unused:UNUSED_PAD src0_sel:DWORD
	v_or3_b32 v4, v1, v6, v8
	v_mul_f32_e32 v6, 0xbcb8aa3b, v40
	v_exp_f32_e32 v6, v6
	v_lshl_or_b32 v1, v9, 8, v7
	v_or3_b32 v5, v1, v11, v10
	global_store_dwordx2 v[2:3], v[4:5], off offset:1536
	v_fma_f32 v4, v6, s98, s98
	v_rcp_f32_e32 v4, v4
	v_mul_f32_e32 v6, 0xbcb8aa3b, v41
	v_exp_f32_e32 v6, v6
	v_min_f32_e32 v4, 0x437f0000, v4
	v_cvt_u32_f32_e32 v7, v4
	v_fma_f32 v4, v6, s98, s98
	v_rcp_f32_e32 v4, v4
	v_mul_f32_e32 v8, 0xbcb8aa3b, v42
	v_exp_f32_e32 v8, v8
	v_mul_f32_e32 v1, 0xbcb8aa3b, v44
	v_mul_f32_e32 v5, 0xbcb8aa3b, v45
	v_min_f32_e32 v4, 0x437f0000, v4
	v_mul_f32_e32 v6, 0xbcb8aa3b, v46
	v_cvt_u32_f32_e32 v9, v4
	v_fma_f32 v4, v8, s98, s98
	v_mul_f32_e32 v8, 0xbcb8aa3b, v47
	v_exp_f32_e32 v1, v1
	v_exp_f32_e32 v5, v5
	v_exp_f32_e32 v6, v6
	v_exp_f32_e32 v8, v8
	v_rcp_f32_e32 v4, v4
	v_mul_f32_e32 v10, 0xbcb8aa3b, v43
	v_fma_f32 v1, v1, s98, s98
	v_fma_f32 v5, v5, s98, s98
	v_rcp_f32_e32 v1, v1
	v_rcp_f32_e32 v5, v5
	v_fma_f32 v6, v6, s98, s98
	v_exp_f32_e32 v10, v10
	v_fma_f32 v8, v8, s98, s98
	v_rcp_f32_e32 v6, v6
	v_rcp_f32_e32 v8, v8
	v_min_f32_e32 v4, 0x437f0000, v4
	v_cvt_u32_f32_sdwa v11, v4 dst_sel:WORD_1 dst_unused:UNUSED_PAD src0_sel:DWORD
	v_fma_f32 v4, v10, s98, s98
	v_min_f32_e32 v1, 0x437f0000, v1
	v_min_f32_e32 v5, 0x437f0000, v5
	v_rcp_f32_e32 v4, v4
	v_cvt_u32_f32_e32 v1, v1
	v_cvt_u32_f32_e32 v5, v5
	v_min_f32_e32 v6, 0x437f0000, v6
	v_min_f32_e32 v8, 0x437f0000, v8
	v_cvt_u32_f32_sdwa v6, v6 dst_sel:WORD_1 dst_unused:UNUSED_PAD src0_sel:DWORD
	v_cvt_u32_f32_sdwa v8, v8 dst_sel:BYTE_3 dst_unused:UNUSED_PAD src0_sel:DWORD
	v_min_f32_e32 v4, 0x437f0000, v4
	v_lshl_or_b32 v1, v5, 8, v1
	v_cvt_u32_f32_sdwa v10, v4 dst_sel:BYTE_3 dst_unused:UNUSED_PAD src0_sel:DWORD
	v_or3_b32 v4, v1, v6, v8
	v_mul_f32_e32 v6, 0xbcb8aa3b, v32
	v_exp_f32_e32 v6, v6
	v_lshl_or_b32 v1, v9, 8, v7
	v_or3_b32 v5, v1, v11, v10
	global_store_dwordx2 v[2:3], v[4:5], off offset:2048
	v_fma_f32 v4, v6, s98, s98
	v_rcp_f32_e32 v4, v4
	v_mul_f32_e32 v6, 0xbcb8aa3b, v33
	v_exp_f32_e32 v6, v6
	v_min_f32_e32 v4, 0x437f0000, v4
	v_cvt_u32_f32_e32 v7, v4
	v_fma_f32 v4, v6, s98, s98
	v_rcp_f32_e32 v4, v4
	v_mul_f32_e32 v8, 0xbcb8aa3b, v34
	v_exp_f32_e32 v8, v8
	v_mul_f32_e32 v1, 0xbcb8aa3b, v36
	v_mul_f32_e32 v5, 0xbcb8aa3b, v37
	v_min_f32_e32 v4, 0x437f0000, v4
	v_mul_f32_e32 v6, 0xbcb8aa3b, v38
	v_cvt_u32_f32_e32 v9, v4
	v_fma_f32 v4, v8, s98, s98
	v_mul_f32_e32 v8, 0xbcb8aa3b, v39
	v_exp_f32_e32 v1, v1
	v_exp_f32_e32 v5, v5
	v_exp_f32_e32 v6, v6
	v_exp_f32_e32 v8, v8
	v_rcp_f32_e32 v4, v4
	v_mul_f32_e32 v10, 0xbcb8aa3b, v35
	v_fma_f32 v1, v1, s98, s98
	v_fma_f32 v5, v5, s98, s98
	v_rcp_f32_e32 v1, v1
	v_rcp_f32_e32 v5, v5
	v_fma_f32 v6, v6, s98, s98
	v_exp_f32_e32 v10, v10
	v_fma_f32 v8, v8, s98, s98
	v_rcp_f32_e32 v6, v6
	v_rcp_f32_e32 v8, v8
	v_min_f32_e32 v4, 0x437f0000, v4
	v_cvt_u32_f32_sdwa v11, v4 dst_sel:WORD_1 dst_unused:UNUSED_PAD src0_sel:DWORD
	v_fma_f32 v4, v10, s98, s98
	v_min_f32_e32 v1, 0x437f0000, v1
	v_min_f32_e32 v5, 0x437f0000, v5
	v_rcp_f32_e32 v4, v4
	v_cvt_u32_f32_e32 v1, v1
	v_cvt_u32_f32_e32 v5, v5
	v_min_f32_e32 v6, 0x437f0000, v6
	v_min_f32_e32 v8, 0x437f0000, v8
	v_cvt_u32_f32_sdwa v6, v6 dst_sel:WORD_1 dst_unused:UNUSED_PAD src0_sel:DWORD
	v_cvt_u32_f32_sdwa v8, v8 dst_sel:BYTE_3 dst_unused:UNUSED_PAD src0_sel:DWORD
	v_min_f32_e32 v4, 0x437f0000, v4
	v_lshl_or_b32 v1, v5, 8, v1
	v_cvt_u32_f32_sdwa v10, v4 dst_sel:BYTE_3 dst_unused:UNUSED_PAD src0_sel:DWORD
	v_or3_b32 v4, v1, v6, v8
	v_mul_f32_e32 v6, 0xbcb8aa3b, v24
	v_exp_f32_e32 v6, v6
	v_lshl_or_b32 v1, v9, 8, v7
	v_or3_b32 v5, v1, v11, v10
	global_store_dwordx2 v[2:3], v[4:5], off offset:2560
	v_fma_f32 v4, v6, s98, s98
	v_rcp_f32_e32 v4, v4
	v_mul_f32_e32 v6, 0xbcb8aa3b, v25
	v_exp_f32_e32 v6, v6
	v_min_f32_e32 v4, 0x437f0000, v4
	v_cvt_u32_f32_e32 v7, v4
	v_fma_f32 v4, v6, s98, s98
	v_rcp_f32_e32 v4, v4
	v_mul_f32_e32 v8, 0xbcb8aa3b, v26
	v_exp_f32_e32 v8, v8
	v_mul_f32_e32 v1, 0xbcb8aa3b, v28
	v_mul_f32_e32 v5, 0xbcb8aa3b, v29
	v_min_f32_e32 v4, 0x437f0000, v4
	v_mul_f32_e32 v6, 0xbcb8aa3b, v30
	v_cvt_u32_f32_e32 v9, v4
	v_fma_f32 v4, v8, s98, s98
	v_mul_f32_e32 v8, 0xbcb8aa3b, v31
	v_exp_f32_e32 v1, v1
	v_exp_f32_e32 v5, v5
	v_exp_f32_e32 v6, v6
	v_exp_f32_e32 v8, v8
	v_rcp_f32_e32 v4, v4
	v_mul_f32_e32 v10, 0xbcb8aa3b, v27
	v_fma_f32 v1, v1, s98, s98
	v_fma_f32 v5, v5, s98, s98
	v_rcp_f32_e32 v1, v1
	v_rcp_f32_e32 v5, v5
	v_fma_f32 v6, v6, s98, s98
	v_exp_f32_e32 v10, v10
	v_fma_f32 v8, v8, s98, s98
	v_rcp_f32_e32 v6, v6
	v_rcp_f32_e32 v8, v8
	v_min_f32_e32 v4, 0x437f0000, v4
	v_cvt_u32_f32_sdwa v11, v4 dst_sel:WORD_1 dst_unused:UNUSED_PAD src0_sel:DWORD
	v_fma_f32 v4, v10, s98, s98
	v_min_f32_e32 v1, 0x437f0000, v1
	v_min_f32_e32 v5, 0x437f0000, v5
	v_rcp_f32_e32 v4, v4
	v_cvt_u32_f32_e32 v1, v1
	v_cvt_u32_f32_e32 v5, v5
	v_min_f32_e32 v6, 0x437f0000, v6
	v_min_f32_e32 v8, 0x437f0000, v8
	v_cvt_u32_f32_sdwa v6, v6 dst_sel:WORD_1 dst_unused:UNUSED_PAD src0_sel:DWORD
	v_cvt_u32_f32_sdwa v8, v8 dst_sel:BYTE_3 dst_unused:UNUSED_PAD src0_sel:DWORD
	v_min_f32_e32 v4, 0x437f0000, v4
	v_lshl_or_b32 v1, v5, 8, v1
	v_cvt_u32_f32_sdwa v10, v4 dst_sel:BYTE_3 dst_unused:UNUSED_PAD src0_sel:DWORD
	v_or3_b32 v4, v1, v6, v8
	v_mul_f32_e32 v6, 0xbcb8aa3b, v16
	v_exp_f32_e32 v6, v6
	v_lshl_or_b32 v1, v9, 8, v7
	v_or3_b32 v5, v1, v11, v10
	global_store_dwordx2 v[2:3], v[4:5], off offset:3072
	v_fma_f32 v4, v6, s98, s98
	v_rcp_f32_e32 v4, v4
	v_mul_f32_e32 v6, 0xbcb8aa3b, v17
	v_exp_f32_e32 v6, v6
	v_min_f32_e32 v4, 0x437f0000, v4
	v_cvt_u32_f32_e32 v7, v4
	v_fma_f32 v4, v6, s98, s98
	v_rcp_f32_e32 v4, v4
	v_mul_f32_e32 v8, 0xbcb8aa3b, v18
	v_exp_f32_e32 v8, v8
	v_mul_f32_e32 v1, 0xbcb8aa3b, v20
	v_mul_f32_e32 v5, 0xbcb8aa3b, v21
	v_min_f32_e32 v4, 0x437f0000, v4
	v_mul_f32_e32 v6, 0xbcb8aa3b, v22
	v_cvt_u32_f32_e32 v9, v4
	v_fma_f32 v4, v8, s98, s98
	v_mul_f32_e32 v8, 0xbcb8aa3b, v23
	v_exp_f32_e32 v1, v1
	v_exp_f32_e32 v5, v5
	v_rcp_f32_e32 v4, v4
	v_mul_f32_e32 v10, 0xbcb8aa3b, v19
	v_exp_f32_e32 v6, v6
	v_exp_f32_e32 v8, v8
	v_exp_f32_e32 v10, v10
	v_fma_f32 v1, v1, s98, s98
	v_fma_f32 v5, v5, s98, s98
	v_rcp_f32_e32 v1, v1
	v_rcp_f32_e32 v5, v5
	v_fma_f32 v6, v6, s98, s98
	v_min_f32_e32 v4, 0x437f0000, v4
	v_fma_f32 v8, v8, s98, s98
	v_rcp_f32_e32 v6, v6
	v_rcp_f32_e32 v8, v8
	v_cvt_u32_f32_sdwa v11, v4 dst_sel:WORD_1 dst_unused:UNUSED_PAD src0_sel:DWORD
	v_fma_f32 v4, v10, s98, s98
	v_rcp_f32_e32 v4, v4
	v_min_f32_e32 v1, 0x437f0000, v1
	v_min_f32_e32 v5, 0x437f0000, v5
	v_cvt_u32_f32_e32 v1, v1
	v_cvt_u32_f32_e32 v5, v5
	v_min_f32_e32 v6, 0x437f0000, v6
	v_min_f32_e32 v8, 0x437f0000, v8
	v_cvt_u32_f32_sdwa v6, v6 dst_sel:WORD_1 dst_unused:UNUSED_PAD src0_sel:DWORD
	v_cvt_u32_f32_sdwa v8, v8 dst_sel:BYTE_3 dst_unused:UNUSED_PAD src0_sel:DWORD
	v_min_f32_e32 v4, 0x437f0000, v4
	v_cvt_u32_f32_sdwa v10, v4 dst_sel:BYTE_3 dst_unused:UNUSED_PAD src0_sel:DWORD
	v_lshl_or_b32 v1, v5, 8, v1
	v_or3_b32 v4, v1, v6, v8
	v_lshl_or_b32 v1, v9, 8, v7
	v_or3_b32 v5, v1, v11, v10
	global_store_dwordx2 v[2:3], v[4:5], off offset:3584

	.amdhsa_kernel _Z3fwd6Params
		.amdhsa_group_segment_fixed_size 0
		.amdhsa_private_segment_fixed_size 0
		.amdhsa_kernarg_size 536
		.amdhsa_user_sgpr_count 2
		.amdhsa_user_sgpr_dispatch_ptr 0
		.amdhsa_user_sgpr_queue_ptr 0
		.amdhsa_user_sgpr_kernarg_segment_ptr 1
		.amdhsa_user_sgpr_dispatch_id 0
		.amdhsa_user_sgpr_kernarg_preload_length 0
		.amdhsa_user_sgpr_kernarg_preload_offset 0
		.amdhsa_user_sgpr_private_segment_size 0
		.amdhsa_uses_dynamic_stack 0
		.amdhsa_enable_private_segment 0
		.amdhsa_system_sgpr_workgroup_id_x 1
		.amdhsa_system_sgpr_workgroup_id_y 0
		.amdhsa_system_sgpr_workgroup_id_z 0
		.amdhsa_system_sgpr_workgroup_info 0
		.amdhsa_system_vgpr_workitem_id 0
		.amdhsa_next_free_vgpr 256
		.amdhsa_next_free_sgpr 99
		.amdhsa_accum_offset 256
		.amdhsa_reserve_vcc 1
		.amdhsa_float_round_mode_32 0
		.amdhsa_float_round_mode_16_64 0
		.amdhsa_float_denorm_mode_32 3
		.amdhsa_float_denorm_mode_16_64 3
		.amdhsa_dx10_clamp 1
		.amdhsa_ieee_mode 1
		.amdhsa_fp16_overflow 0
		.amdhsa_tg_split 0
		.amdhsa_exception_fp_ieee_invalid_op 0
		.amdhsa_exception_fp_denorm_src 0
		.amdhsa_exception_fp_ieee_div_zero 0
		.amdhsa_exception_fp_ieee_overflow 0
		.amdhsa_exception_fp_ieee_underflow 0
		.amdhsa_exception_fp_ieee_inexact 0
		.amdhsa_exception_int_div_zero 0
	.end_amdhsa_kernel

amdhsa.kernels:
  - .agpr_count:     0
    .args:
      - .offset:         0
        .size:           280
        .value_kind:     by_value
      - .offset:         280
        .size:           4
        .value_kind:     hidden_block_count_x
      - .offset:         284
        .size:           4
        .value_kind:     hidden_block_count_y
      - .offset:         288
        .size:           4
        .value_kind:     hidden_block_count_z
      - .offset:         292
        .size:           2
        .value_kind:     hidden_group_size_x
      - .offset:         294
        .size:           2
        .value_kind:     hidden_group_size_y
      - .offset:         296
        .size:           2
        .value_kind:     hidden_group_size_z
      - .offset:         298
        .size:           2
        .value_kind:     hidden_remainder_x
      - .offset:         300
        .size:           2
        .value_kind:     hidden_remainder_y
      - .offset:         302
        .size:           2
        .value_kind:     hidden_remainder_z
      - .offset:         320
        .size:           8
        .value_kind:     hidden_global_offset_x
      - .offset:         328
        .size:           8
        .value_kind:     hidden_global_offset_y
      - .offset:         336
        .size:           8
        .value_kind:     hidden_global_offset_z
      - .offset:         344
        .size:           2
        .value_kind:     hidden_grid_dims
      - .offset:         400
        .size:           4
        .value_kind:     hidden_dynamic_lds_size
    .group_segment_fixed_size: 0
    .kernarg_segment_align: 8
    .kernarg_segment_size: 536
    .language:       OpenCL C
    .language_version:
      - 2
      - 0
    .max_flat_workgroup_size: 512
    .name:           _Z3fwd6Params
    .private_segment_fixed_size: 0
    .sgpr_count:     105
    .sgpr_spill_count: 5
    .symbol:         _Z3fwd6Params.kd
    .uniform_work_group_size: 1
    .uses_dynamic_stack: false
    .vgpr_count:     256
    .vgpr_spill_count: 0
    .wavefront_size: 64
